# v13 plus: out-proj and dense-down residual epilogues issue the second half's residual loads right after the first half's (7 of 8, spare fragment registers), copied into place later
# baseline (speedup 1.0000x reference)
.LBB0_544:
	s_lshl_b32 s30, s57, 8
	v_mov_b32_e32 v150, v1
	v_mov_b32_e32 v132, v189
	s_lshl_b32 s14, s56, 8
	s_or_b32 s30, s30, s50
	s_add_i32 s14, s14, s49
	v_lshl_add_u32 v148, v132, 3, s30
	s_ashr_i32 s30, s56, 3
	s_mul_hi_i32 s31, s30, 0x6000
	s_mulk_i32 s30, 0x6000
	v_ashrrev_i32_e32 v149, 31, v148
	v_add_u32_e32 v150, s14, v150
	s_add_u32 s30, s47, s30
	v_lshlrev_b64 v[200:201], 1, v[148:149]
	v_ashrrev_i32_e32 v151, 31, v150
	s_addc_u32 s31, s48, s31
	v_lshl_add_u64 v[202:203], s[80:81], 0, v[200:201]
	v_lshlrev_b64 v[204:205], 11, v[150:151]
	v_lshl_add_u64 v[136:137], v[148:149], 2, s[30:31]
	v_lshl_add_u64 v[148:149], v[202:203], 0, v[204:205]
	global_load_dwordx4 v[140:143], v[136:137], off offset:16
	global_load_dwordx4 v[144:147], v[136:137], off
	global_load_dwordx4 v[132:135], v[136:137], off offset:528
	s_nop 0
	global_load_dwordx4 v[136:139], v[136:137], off offset:512
	s_nop 0
	global_load_dwordx4 v[178:181], v[148:149], off
	global_load_dwordx4 v[172:175], v[148:149], off offset:256
	s_mov_b64 s[24:25], 0x8000
	v_lshl_add_u64 v[210:211], v[204:205], 0, s[24:25]
	v_lshl_add_u64 v[148:149], v[202:203], 0, v[210:211]
	global_load_dwordx4 v[168:171], v[148:149], off
	global_load_dwordx4 v[164:167], v[148:149], off offset:256
	s_mov_b64 s[24:25], 0x10000
	v_lshl_add_u64 v[208:209], v[204:205], 0, s[24:25]
	v_lshl_add_u64 v[148:149], v[202:203], 0, v[208:209]
	global_load_dwordx4 v[160:163], v[148:149], off
	global_load_dwordx4 v[156:159], v[148:149], off offset:256
	s_mov_b64 s[24:25], 0x18000
	v_lshl_add_u64 v[206:207], v[204:205], 0, s[24:25]
	v_lshl_add_u64 v[148:149], v[202:203], 0, v[206:207]
	global_load_dwordx4 v[152:155], v[148:149], off
	s_nop 0
	global_load_dwordx4 v[148:151], v[148:149], off offset:256
	s_mov_b64 s[98:99], 0x40000
	v_lshl_add_u64 v[244:245], v[204:205], 0, s[98:99]
	v_lshl_add_u64 v[244:245], v[202:203], 0, v[244:245]
	global_load_dwordx4 v[212:215], v[244:245], off
	global_load_dwordx4 v[216:219], v[244:245], off offset:256
	s_mov_b64 s[98:99], 0x48000
	v_lshl_add_u64 v[244:245], v[204:205], 0, s[98:99]
	v_lshl_add_u64 v[244:245], v[202:203], 0, v[244:245]
	global_load_dwordx4 v[224:227], v[244:245], off
	global_load_dwordx4 v[228:231], v[244:245], off offset:256
	s_mov_b64 s[98:99], 0x50000
	v_lshl_add_u64 v[244:245], v[204:205], 0, s[98:99]
	v_lshl_add_u64 v[244:245], v[202:203], 0, v[244:245]
	global_load_dwordx4 v[232:235], v[244:245], off
	global_load_dwordx4 v[236:239], v[244:245], off offset:256
	s_mov_b64 s[98:99], 0x58000
	v_lshl_add_u64 v[244:245], v[204:205], 0, s[98:99]
	v_lshl_add_u64 v[244:245], v[202:203], 0, v[244:245]
	global_load_dwordx4 v[240:243], v[244:245], off
	s_mov_b64 s[24:25], 0x40000
	v_readlane_b32 s76, v255, 5
	s_mov_b64 s[30:31], -1
	s_andn2_b64 vcc, exec, s[4:5]
	v_readlane_b32 s77, v255, 6
	s_waitcnt vmcnt(7)
	v_lshlrev_b32_e32 v182, 16, v178
	v_and_b32_e32 v183, 0xffff0000, v178
	v_pk_fma_f32 v[182:183], v[128:129], v[144:145], v[182:183]
	s_nop 0
	v_cvt_pk_bf16_f32 v178, v182, v183
	v_lshlrev_b32_e32 v182, 16, v179
	v_and_b32_e32 v183, 0xffff0000, v179
	v_pk_fma_f32 v[182:183], v[130:131], v[146:147], v[182:183]
	s_nop 0
	v_cvt_pk_bf16_f32 v179, v182, v183
	v_lshlrev_b32_e32 v182, 16, v180
	v_and_b32_e32 v183, 0xffff0000, v180
	v_pk_fma_f32 v[182:183], v[124:125], v[140:141], v[182:183]
	s_nop 0
	v_cvt_pk_bf16_f32 v180, v182, v183
	v_lshlrev_b32_e32 v182, 16, v181
	v_and_b32_e32 v183, 0xffff0000, v181
	v_pk_fma_f32 v[182:183], v[126:127], v[142:143], v[182:183]
	s_nop 0
	v_cvt_pk_bf16_f32 v181, v182, v183
	v_lshl_add_u64 v[182:183], s[8:9], 0, v[204:205]
	v_lshl_add_u64 v[182:183], v[182:183], 0, v[200:201]
	global_store_dwordx4 v[182:183], v[178:181], off
	s_nop 1
	v_lshlrev_b32_e32 v178, 16, v172
	v_and_b32_e32 v179, 0xffff0000, v172
	v_pk_fma_f32 v[178:179], v[96:97], v[136:137], v[178:179]
	s_nop 0
	v_cvt_pk_bf16_f32 v172, v178, v179
	v_lshlrev_b32_e32 v178, 16, v173
	v_and_b32_e32 v179, 0xffff0000, v173
	v_pk_fma_f32 v[178:179], v[98:99], v[138:139], v[178:179]
	s_nop 0
	v_cvt_pk_bf16_f32 v173, v178, v179
	v_lshlrev_b32_e32 v178, 16, v174
	v_and_b32_e32 v179, 0xffff0000, v174
	v_pk_fma_f32 v[178:179], v[92:93], v[132:133], v[178:179]
	s_nop 0
	v_cvt_pk_bf16_f32 v174, v178, v179
	v_lshlrev_b32_e32 v178, 16, v175
	v_and_b32_e32 v179, 0xffff0000, v175
	v_pk_fma_f32 v[178:179], v[94:95], v[134:135], v[178:179]
	s_nop 0
	v_cvt_pk_bf16_f32 v175, v178, v179
	global_store_dwordx4 v[182:183], v[172:175], off offset:256
	v_lshl_add_u64 v[182:183], v[204:205], 0, s[24:25]
	s_mov_b64 s[24:25], 0x48000
	v_lshlrev_b32_e32 v172, 16, v168
	v_and_b32_e32 v173, 0xffff0000, v168
	v_pk_fma_f32 v[172:173], v[120:121], v[144:145], v[172:173]
	v_lshl_add_u64 v[184:185], v[204:205], 0, s[24:25]
	v_cvt_pk_bf16_f32 v168, v172, v173
	v_lshlrev_b32_e32 v172, 16, v169
	v_and_b32_e32 v173, 0xffff0000, v169
	v_pk_fma_f32 v[172:173], v[122:123], v[146:147], v[172:173]
	s_mov_b64 s[24:25], 0x50000
	v_cvt_pk_bf16_f32 v169, v172, v173
	v_lshlrev_b32_e32 v172, 16, v170
	v_and_b32_e32 v173, 0xffff0000, v170
	v_pk_fma_f32 v[172:173], v[116:117], v[140:141], v[172:173]
	s_nop 0
	v_cvt_pk_bf16_f32 v170, v172, v173
	v_lshlrev_b32_e32 v172, 16, v171
	v_and_b32_e32 v173, 0xffff0000, v171
	v_pk_fma_f32 v[172:173], v[118:119], v[142:143], v[172:173]
	s_nop 0
	v_cvt_pk_bf16_f32 v171, v172, v173
	v_lshl_add_u64 v[172:173], s[8:9], 0, v[210:211]
	v_lshl_add_u64 v[172:173], v[172:173], 0, v[200:201]
	global_store_dwordx4 v[172:173], v[168:171], off
	s_nop 1
	v_lshlrev_b32_e32 v168, 16, v164
	v_and_b32_e32 v169, 0xffff0000, v164
	v_pk_fma_f32 v[168:169], v[88:89], v[136:137], v[168:169]
	s_nop 0
	v_cvt_pk_bf16_f32 v164, v168, v169
	v_lshlrev_b32_e32 v168, 16, v165
	v_and_b32_e32 v169, 0xffff0000, v165
	v_pk_fma_f32 v[168:169], v[90:91], v[138:139], v[168:169]
	s_nop 0
	v_cvt_pk_bf16_f32 v165, v168, v169
	v_lshlrev_b32_e32 v168, 16, v166
	v_and_b32_e32 v169, 0xffff0000, v166
	v_pk_fma_f32 v[168:169], v[84:85], v[132:133], v[168:169]
	s_nop 0
	v_cvt_pk_bf16_f32 v166, v168, v169
	v_lshlrev_b32_e32 v168, 16, v167
	v_and_b32_e32 v169, 0xffff0000, v167
	v_pk_fma_f32 v[168:169], v[86:87], v[134:135], v[168:169]
	s_nop 0
	v_cvt_pk_bf16_f32 v167, v168, v169
	global_store_dwordx4 v[172:173], v[164:167], off offset:256
	s_nop 1
	v_lshlrev_b32_e32 v164, 16, v160
	v_and_b32_e32 v165, 0xffff0000, v160
	v_pk_fma_f32 v[164:165], v[112:113], v[144:145], v[164:165]
	s_nop 0
	v_cvt_pk_bf16_f32 v160, v164, v165
	v_lshlrev_b32_e32 v164, 16, v161
	v_and_b32_e32 v165, 0xffff0000, v161
	v_pk_fma_f32 v[164:165], v[114:115], v[146:147], v[164:165]
	s_nop 0
	v_cvt_pk_bf16_f32 v161, v164, v165
	v_lshlrev_b32_e32 v164, 16, v162
	v_and_b32_e32 v165, 0xffff0000, v162
	v_pk_fma_f32 v[164:165], v[108:109], v[140:141], v[164:165]
	s_nop 0
	v_cvt_pk_bf16_f32 v162, v164, v165
	v_lshlrev_b32_e32 v164, 16, v163
	v_and_b32_e32 v165, 0xffff0000, v163
	v_pk_fma_f32 v[164:165], v[110:111], v[142:143], v[164:165]
	s_nop 0
	v_cvt_pk_bf16_f32 v163, v164, v165
	v_lshl_add_u64 v[164:165], s[8:9], 0, v[208:209]
	v_lshl_add_u64 v[164:165], v[164:165], 0, v[200:201]
	global_store_dwordx4 v[164:165], v[160:163], off
	s_nop 1
	v_lshlrev_b32_e32 v160, 16, v156
	v_and_b32_e32 v161, 0xffff0000, v156
	v_pk_fma_f32 v[160:161], v[80:81], v[136:137], v[160:161]
	s_nop 0
	v_cvt_pk_bf16_f32 v156, v160, v161
	v_lshlrev_b32_e32 v160, 16, v157
	v_and_b32_e32 v161, 0xffff0000, v157
	v_pk_fma_f32 v[160:161], v[82:83], v[138:139], v[160:161]
	s_nop 0
	v_cvt_pk_bf16_f32 v157, v160, v161
	v_lshlrev_b32_e32 v160, 16, v158
	v_and_b32_e32 v161, 0xffff0000, v158
	v_pk_fma_f32 v[160:161], v[76:77], v[132:133], v[160:161]
	s_nop 0
	v_cvt_pk_bf16_f32 v158, v160, v161
	v_lshlrev_b32_e32 v160, 16, v159
	v_and_b32_e32 v161, 0xffff0000, v159
	v_pk_fma_f32 v[160:161], v[78:79], v[134:135], v[160:161]
	s_nop 0
	v_cvt_pk_bf16_f32 v159, v160, v161
	global_store_dwordx4 v[164:165], v[156:159], off offset:256
	s_nop 1
	v_lshlrev_b32_e32 v156, 16, v152
	v_and_b32_e32 v157, 0xffff0000, v152
	v_pk_fma_f32 v[156:157], v[104:105], v[144:145], v[156:157]
	s_nop 0
	v_cvt_pk_bf16_f32 v152, v156, v157
	v_lshlrev_b32_e32 v156, 16, v153
	v_and_b32_e32 v157, 0xffff0000, v153
	v_pk_fma_f32 v[156:157], v[106:107], v[146:147], v[156:157]
	s_nop 0
	v_cvt_pk_bf16_f32 v153, v156, v157
	v_lshlrev_b32_e32 v156, 16, v154
	v_and_b32_e32 v157, 0xffff0000, v154
	v_pk_fma_f32 v[156:157], v[100:101], v[140:141], v[156:157]
	s_nop 0
	v_cvt_pk_bf16_f32 v154, v156, v157
	v_lshlrev_b32_e32 v156, 16, v155
	v_and_b32_e32 v157, 0xffff0000, v155
	v_pk_fma_f32 v[156:157], v[102:103], v[142:143], v[156:157]
	s_nop 0
	v_cvt_pk_bf16_f32 v155, v156, v157
	v_lshl_add_u64 v[156:157], s[8:9], 0, v[206:207]
	v_lshl_add_u64 v[156:157], v[156:157], 0, v[200:201]
	global_store_dwordx4 v[156:157], v[152:155], off
	v_lshl_add_u64 v[206:207], v[204:205], 0, s[24:25]
	s_mov_b64 s[24:25], 0x58000
	v_lshlrev_b32_e32 v152, 16, v148
	v_and_b32_e32 v153, 0xffff0000, v148
	v_pk_fma_f32 v[152:153], v[72:73], v[136:137], v[152:153]
	v_lshl_add_u64 v[204:205], v[204:205], 0, s[24:25]
	v_cvt_pk_bf16_f32 v148, v152, v153
	v_lshlrev_b32_e32 v152, 16, v149
	v_and_b32_e32 v153, 0xffff0000, v149
	v_pk_fma_f32 v[152:153], v[74:75], v[138:139], v[152:153]
	s_nop 0
	v_cvt_pk_bf16_f32 v149, v152, v153
	v_lshlrev_b32_e32 v152, 16, v150
	v_and_b32_e32 v153, 0xffff0000, v150
	v_pk_fma_f32 v[152:153], v[68:69], v[132:133], v[152:153]
	s_nop 0
	v_cvt_pk_bf16_f32 v150, v152, v153
	v_lshlrev_b32_e32 v152, 16, v151
	v_and_b32_e32 v153, 0xffff0000, v151
	v_pk_fma_f32 v[152:153], v[70:71], v[134:135], v[152:153]
	s_nop 0
	v_cvt_pk_bf16_f32 v151, v152, v153
	global_store_dwordx4 v[156:157], v[148:151], off offset:256
	s_nop 1
	v_lshl_add_u64 v[148:149], v[202:203], 0, v[182:183]
	s_waitcnt vmcnt(8)
	v_mov_b64_e32 v[152:153], v[212:213]
	v_mov_b64_e32 v[154:155], v[214:215]
	v_mov_b64_e32 v[156:157], v[216:217]
	v_mov_b64_e32 v[158:159], v[218:219]
	v_lshl_add_u64 v[148:149], v[202:203], 0, v[184:185]
	v_mov_b64_e32 v[160:161], v[224:225]
	v_mov_b64_e32 v[162:163], v[226:227]
	v_mov_b64_e32 v[164:165], v[228:229]
	v_mov_b64_e32 v[166:167], v[230:231]
	v_lshl_add_u64 v[148:149], v[202:203], 0, v[206:207]
	v_mov_b64_e32 v[168:169], v[232:233]
	v_mov_b64_e32 v[170:171], v[234:235]
	v_mov_b64_e32 v[172:173], v[236:237]
	v_mov_b64_e32 v[174:175], v[238:239]
	v_lshl_add_u64 v[148:149], v[202:203], 0, v[204:205]
	v_mov_b64_e32 v[178:179], v[240:241]
	v_mov_b64_e32 v[180:181], v[242:243]
	s_nop 0
	global_load_dwordx4 v[148:151], v[148:149], off offset:256
	v_lshl_add_u64 v[182:183], s[8:9], 0, v[182:183]
	v_lshl_add_u64 v[182:183], v[182:183], 0, v[200:201]
	s_waitcnt vmcnt(7)
	v_lshlrev_b32_e32 v202, 16, v152
	v_and_b32_e32 v203, 0xffff0000, v152
	v_pk_fma_f32 v[202:203], v[64:65], v[144:145], v[202:203]
	s_nop 0
	v_cvt_pk_bf16_f32 v152, v202, v203
	v_lshlrev_b32_e32 v202, 16, v153
	v_and_b32_e32 v203, 0xffff0000, v153
	v_pk_fma_f32 v[202:203], v[66:67], v[146:147], v[202:203]
	s_nop 0
	v_cvt_pk_bf16_f32 v153, v202, v203
	v_lshlrev_b32_e32 v202, 16, v154
	v_and_b32_e32 v203, 0xffff0000, v154
	v_pk_fma_f32 v[202:203], v[60:61], v[140:141], v[202:203]
	s_nop 0
	v_cvt_pk_bf16_f32 v154, v202, v203
	v_lshlrev_b32_e32 v202, 16, v155
	v_and_b32_e32 v203, 0xffff0000, v155
	v_pk_fma_f32 v[202:203], v[62:63], v[142:143], v[202:203]
	s_nop 0
	v_cvt_pk_bf16_f32 v155, v202, v203
	global_store_dwordx4 v[182:183], v[152:155], off
	s_waitcnt vmcnt(7)
	s_nop 0
	v_lshlrev_b32_e32 v152, 16, v156
	v_and_b32_e32 v153, 0xffff0000, v156
	v_lshlrev_b32_e32 v154, 16, v157
	v_and_b32_e32 v155, 0xffff0000, v157
	v_pk_fma_f32 v[152:153], v[30:31], v[136:137], v[152:153]
	v_pk_fma_f32 v[154:155], v[32:33], v[138:139], v[154:155]
	v_cvt_pk_bf16_f32 v152, v152, v153
	v_cvt_pk_bf16_f32 v153, v154, v155
	v_lshlrev_b32_e32 v154, 16, v158
	v_and_b32_e32 v155, 0xffff0000, v158
	v_lshlrev_b32_e32 v156, 16, v159
	v_and_b32_e32 v157, 0xffff0000, v159
	v_pk_fma_f32 v[154:155], v[26:27], v[132:133], v[154:155]
	v_pk_fma_f32 v[156:157], v[28:29], v[134:135], v[156:157]
	v_cvt_pk_bf16_f32 v154, v154, v155
	v_cvt_pk_bf16_f32 v155, v156, v157
	global_store_dwordx4 v[182:183], v[152:155], off offset:256
	s_waitcnt vmcnt(7)
	v_lshlrev_b32_e32 v156, 16, v163
	v_and_b32_e32 v157, 0xffff0000, v163
	v_lshlrev_b32_e32 v152, 16, v160
	v_and_b32_e32 v153, 0xffff0000, v160
	v_lshlrev_b32_e32 v154, 16, v161
	v_and_b32_e32 v155, 0xffff0000, v161
	v_pk_fma_f32 v[152:153], v[56:57], v[144:145], v[152:153]
	v_pk_fma_f32 v[154:155], v[58:59], v[146:147], v[154:155]
	v_cvt_pk_bf16_f32 v152, v152, v153
	v_cvt_pk_bf16_f32 v153, v154, v155
	v_lshlrev_b32_e32 v154, 16, v162
	v_and_b32_e32 v155, 0xffff0000, v162
	v_pk_fma_f32 v[154:155], v[52:53], v[140:141], v[154:155]
	v_pk_fma_f32 v[156:157], v[54:55], v[142:143], v[156:157]
	v_cvt_pk_bf16_f32 v154, v154, v155
	v_cvt_pk_bf16_f32 v155, v156, v157
	v_lshl_add_u64 v[156:157], s[8:9], 0, v[184:185]
	v_lshl_add_u64 v[156:157], v[156:157], 0, v[200:201]
	global_store_dwordx4 v[156:157], v[152:155], off
	s_waitcnt vmcnt(7)
	v_lshlrev_b32_e32 v158, 16, v167
	v_and_b32_e32 v159, 0xffff0000, v167
	v_lshlrev_b32_e32 v152, 16, v164
	v_and_b32_e32 v153, 0xffff0000, v164
	v_lshlrev_b32_e32 v154, 16, v165
	v_and_b32_e32 v155, 0xffff0000, v165
	v_pk_fma_f32 v[152:153], v[22:23], v[136:137], v[152:153]
	v_pk_fma_f32 v[154:155], v[24:25], v[138:139], v[154:155]
	v_cvt_pk_bf16_f32 v152, v152, v153
	v_cvt_pk_bf16_f32 v153, v154, v155
	v_lshlrev_b32_e32 v154, 16, v166
	v_and_b32_e32 v155, 0xffff0000, v166
	v_pk_fma_f32 v[154:155], v[18:19], v[132:133], v[154:155]
	v_pk_fma_f32 v[158:159], v[20:21], v[134:135], v[158:159]
	v_cvt_pk_bf16_f32 v154, v154, v155
	v_cvt_pk_bf16_f32 v155, v158, v159
	global_store_dwordx4 v[156:157], v[152:155], off offset:256
	s_waitcnt vmcnt(7)
	v_lshlrev_b32_e32 v156, 16, v171
	v_and_b32_e32 v157, 0xffff0000, v171
	v_lshlrev_b32_e32 v152, 16, v168
	v_and_b32_e32 v153, 0xffff0000, v168
	v_lshlrev_b32_e32 v154, 16, v169
	v_and_b32_e32 v155, 0xffff0000, v169
	v_pk_fma_f32 v[152:153], v[48:49], v[144:145], v[152:153]
	v_pk_fma_f32 v[154:155], v[50:51], v[146:147], v[154:155]
	v_cvt_pk_bf16_f32 v152, v152, v153
	v_cvt_pk_bf16_f32 v153, v154, v155
	v_lshlrev_b32_e32 v154, 16, v170
	v_and_b32_e32 v155, 0xffff0000, v170
	v_pk_fma_f32 v[154:155], v[44:45], v[140:141], v[154:155]
	v_pk_fma_f32 v[156:157], v[46:47], v[142:143], v[156:157]
	v_cvt_pk_bf16_f32 v154, v154, v155
	v_cvt_pk_bf16_f32 v155, v156, v157
	v_lshl_add_u64 v[156:157], s[8:9], 0, v[206:207]
	v_lshl_add_u64 v[156:157], v[156:157], 0, v[200:201]
	global_store_dwordx4 v[156:157], v[152:155], off
	s_waitcnt vmcnt(7)
	v_lshlrev_b32_e32 v158, 16, v175
	v_and_b32_e32 v159, 0xffff0000, v175
	v_lshlrev_b32_e32 v152, 16, v172
	v_and_b32_e32 v153, 0xffff0000, v172
	v_lshlrev_b32_e32 v154, 16, v173
	v_and_b32_e32 v155, 0xffff0000, v173
	v_pk_fma_f32 v[152:153], v[14:15], v[136:137], v[152:153]
	v_pk_fma_f32 v[154:155], v[16:17], v[138:139], v[154:155]
	v_cvt_pk_bf16_f32 v152, v152, v153
	v_cvt_pk_bf16_f32 v153, v154, v155
	v_lshlrev_b32_e32 v154, 16, v174
	v_and_b32_e32 v155, 0xffff0000, v174
	v_pk_fma_f32 v[154:155], v[10:11], v[132:133], v[154:155]
	v_pk_fma_f32 v[158:159], v[12:13], v[134:135], v[158:159]
	v_cvt_pk_bf16_f32 v154, v154, v155
	v_cvt_pk_bf16_f32 v155, v158, v159
	global_store_dwordx4 v[156:157], v[152:155], off offset:256
	s_waitcnt vmcnt(7)
	s_nop 0
	v_lshlrev_b32_e32 v152, 16, v178
	v_and_b32_e32 v153, 0xffff0000, v178
	v_pk_fma_f32 v[144:145], v[40:41], v[144:145], v[152:153]
	v_lshlrev_b32_e32 v152, 16, v179
	v_and_b32_e32 v153, 0xffff0000, v179
	v_pk_fma_f32 v[146:147], v[42:43], v[146:147], v[152:153]
	v_cvt_pk_bf16_f32 v144, v144, v145
	v_cvt_pk_bf16_f32 v145, v146, v147
	v_lshlrev_b32_e32 v146, 16, v180
	v_and_b32_e32 v147, 0xffff0000, v180
	v_pk_fma_f32 v[140:141], v[36:37], v[140:141], v[146:147]
	s_nop 0
	v_cvt_pk_bf16_f32 v146, v140, v141
	v_lshlrev_b32_e32 v140, 16, v181
	v_and_b32_e32 v141, 0xffff0000, v181
	v_pk_fma_f32 v[140:141], v[38:39], v[142:143], v[140:141]
	s_waitcnt vmcnt(6)
	v_lshlrev_b32_e32 v142, 16, v148
	v_and_b32_e32 v143, 0xffff0000, v148
	v_pk_fma_f32 v[136:137], v[6:7], v[136:137], v[142:143]
	v_lshlrev_b32_e32 v142, 16, v149
	v_and_b32_e32 v143, 0xffff0000, v149
	v_pk_fma_f32 v[138:139], v[8:9], v[138:139], v[142:143]
	v_cvt_pk_bf16_f32 v136, v136, v137
	v_cvt_pk_bf16_f32 v137, v138, v139
	v_lshlrev_b32_e32 v138, 16, v150
	v_and_b32_e32 v139, 0xffff0000, v150
	v_pk_fma_f32 v[132:133], v[2:3], v[132:133], v[138:139]
	v_cvt_pk_bf16_f32 v147, v140, v141
	v_cvt_pk_bf16_f32 v138, v132, v133
	v_lshlrev_b32_e32 v132, 16, v151
	v_and_b32_e32 v133, 0xffff0000, v151
	v_lshl_add_u64 v[140:141], s[8:9], 0, v[204:205]
	v_pk_fma_f32 v[132:133], v[4:5], v[134:135], v[132:133]
	v_lshl_add_u64 v[140:141], v[140:141], 0, v[200:201]
	v_cvt_pk_bf16_f32 v139, v132, v133
	global_store_dwordx4 v[140:141], v[144:147], off
	global_store_dwordx4 v[140:141], v[136:139], off offset:256
	s_cbranch_vccnz .LBB0_533
	s_andn2_b64 vcc, exec, s[6:7]
	s_cbranch_vccnz .LBB0_532
	s_barrier
	s_branch .LBB0_532

.LBB0_1163:
	s_lshl_b32 s22, s57, 8
	v_mov_b32_e32 v14, v1
	v_mov_b32_e32 v2, v189
	s_or_b32 s22, s22, s50
	s_nop 15
	s_nop 15
	s_lshl_b32 s14, s56, 8
	v_lshl_add_u32 v10, v2, 3, s22
	s_ashr_i32 s22, s56, 3
	s_add_i32 s14, s14, s49
	s_mul_hi_i32 s23, s22, 0x6000
	s_mulk_i32 s22, 0x6000
	s_add_u32 s22, s47, s22
	s_addc_u32 s23, s48, s23
	v_ashrrev_i32_e32 v11, 31, v10
	v_lshl_add_u64 v[12:13], v[10:11], 2, s[22:23]
	global_load_dwordx4 v[2:5], v[12:13], off offset:16
	global_load_dwordx4 v[6:9], v[12:13], off
	s_mov_b32 s64, 0x3b000000
	v_lshlrev_b64 v[200:201], 1, v[10:11]
	v_lshl_add_u64 v[202:203], s[80:81], 0, v[200:201]
	s_mov_b64 s[22:23], 0x8000
	s_andn2_b64 vcc, exec, s[4:5]
	s_waitcnt vmcnt(0)
	v_pk_mul_f32 v[174:175], v[4:5], s[64:65] op_sel_hi:[1,0]
	v_pk_mul_f32 v[196:197], v[8:9], s[64:65] op_sel_hi:[1,0]
	v_pk_mul_f32 v[198:199], v[6:7], s[64:65] op_sel_hi:[1,0]
	v_pk_mul_f32 v[192:193], v[2:3], s[64:65] op_sel_hi:[1,0]
	global_load_dwordx4 v[2:5], v[12:13], off offset:528
	global_load_dwordx4 v[6:9], v[12:13], off offset:512
	s_waitcnt vmcnt(1)
	v_pk_mul_f32 v[32:33], v[2:3], s[64:65] op_sel_hi:[1,0]
	v_add_u32_e32 v2, s14, v14
	v_ashrrev_i32_e32 v3, 31, v2
	v_lshlrev_b64 v[204:205], 11, v[2:3]
	v_lshl_add_u64 v[2:3], v[202:203], 0, v[204:205]
	global_load_dwordx4 v[178:181], v[2:3], off
	global_load_dwordx4 v[26:29], v[2:3], off offset:256
	v_lshl_add_u64 v[210:211], v[204:205], 0, s[22:23]
	v_lshl_add_u64 v[2:3], v[202:203], 0, v[210:211]
	global_load_dwordx4 v[22:25], v[2:3], off
	global_load_dwordx4 v[18:21], v[2:3], off offset:256
	s_mov_b64 s[22:23], 0x10000
	v_lshl_add_u64 v[208:209], v[204:205], 0, s[22:23]
	v_lshl_add_u64 v[2:3], v[202:203], 0, v[208:209]
	global_load_dwordx4 v[14:17], v[2:3], off
	global_load_dwordx4 v[10:13], v[2:3], off offset:256
	s_mov_b64 s[22:23], 0x18000
	v_lshl_add_u64 v[206:207], v[204:205], 0, s[22:23]
	v_lshl_add_u64 v[2:3], v[202:203], 0, v[206:207]
	s_waitcnt vmcnt(6)
	v_pk_mul_f32 v[190:191], v[8:9], s[64:65] op_sel_hi:[1,0]
	v_pk_mul_f32 v[194:195], v[6:7], s[64:65] op_sel_hi:[1,0]
	v_pk_mul_f32 v[30:31], v[4:5], s[64:65] op_sel_hi:[1,0]
	global_load_dwordx4 v[6:9], v[2:3], off
	s_nop 0
	global_load_dwordx4 v[2:5], v[2:3], off offset:256
	s_mov_b64 s[98:99], 0x40000
	v_lshl_add_u64 v[244:245], v[204:205], 0, s[98:99]
	v_lshl_add_u64 v[244:245], v[202:203], 0, v[244:245]
	global_load_dwordx4 v[212:215], v[244:245], off
	global_load_dwordx4 v[216:219], v[244:245], off offset:256
	s_mov_b64 s[98:99], 0x48000
	v_lshl_add_u64 v[244:245], v[204:205], 0, s[98:99]
	v_lshl_add_u64 v[244:245], v[202:203], 0, v[244:245]
	global_load_dwordx4 v[224:227], v[244:245], off
	global_load_dwordx4 v[228:231], v[244:245], off offset:256
	s_mov_b64 s[98:99], 0x50000
	v_lshl_add_u64 v[244:245], v[204:205], 0, s[98:99]
	v_lshl_add_u64 v[244:245], v[202:203], 0, v[244:245]
	global_load_dwordx4 v[232:235], v[244:245], off
	global_load_dwordx4 v[236:239], v[244:245], off offset:256
	s_mov_b64 s[98:99], 0x58000
	v_lshl_add_u64 v[244:245], v[204:205], 0, s[98:99]
	v_lshl_add_u64 v[244:245], v[202:203], 0, v[244:245]
	global_load_dwordx4 v[240:243], v[244:245], off
	s_mov_b64 s[22:23], 0x40000
	s_waitcnt vmcnt(14)
	v_lshlrev_b32_e32 v182, 16, v178
	v_and_b32_e32 v183, 0xffff0000, v178
	v_lshlrev_b32_e32 v178, 16, v179
	v_and_b32_e32 v179, 0xffff0000, v179
	v_pk_fma_f32 v[160:161], v[160:161], v[198:199], v[182:183]
	v_pk_fma_f32 v[162:163], v[162:163], v[196:197], v[178:179]
	v_cvt_pk_bf16_f32 v160, v160, v161
	v_cvt_pk_bf16_f32 v161, v162, v163
	v_lshlrev_b32_e32 v162, 16, v180
	v_and_b32_e32 v163, 0xffff0000, v180
	v_pk_fma_f32 v[156:157], v[156:157], v[192:193], v[162:163]
	s_nop 0
	v_cvt_pk_bf16_f32 v162, v156, v157
	v_lshlrev_b32_e32 v156, 16, v181
	v_and_b32_e32 v157, 0xffff0000, v181
	v_pk_fma_f32 v[156:157], v[158:159], v[174:175], v[156:157]
	s_waitcnt vmcnt(13)
	v_lshlrev_b32_e32 v158, 16, v26
	v_and_b32_e32 v159, 0xffff0000, v26
	v_pk_fma_f32 v[152:153], v[152:153], v[194:195], v[158:159]
	v_cvt_pk_bf16_f32 v163, v156, v157
	v_cvt_pk_bf16_f32 v26, v152, v153
	v_lshlrev_b32_e32 v152, 16, v27
	v_and_b32_e32 v153, 0xffff0000, v27
	v_pk_fma_f32 v[152:153], v[154:155], v[190:191], v[152:153]
	v_lshl_add_u64 v[156:157], s[80:81], 0, v[204:205]
	v_cvt_pk_bf16_f32 v27, v152, v153
	v_lshlrev_b32_e32 v152, 16, v28
	v_and_b32_e32 v153, 0xffff0000, v28
	v_pk_fma_f32 v[148:149], v[148:149], v[32:33], v[152:153]
	v_lshl_add_u64 v[156:157], v[156:157], 0, v[200:201]
	v_cvt_pk_bf16_f32 v28, v148, v149
	v_lshlrev_b32_e32 v148, 16, v29
	v_and_b32_e32 v149, 0xffff0000, v29
	v_pk_fma_f32 v[148:149], v[150:151], v[30:31], v[148:149]
	global_store_dwordx4 v[156:157], v[160:163], off
	v_cvt_pk_bf16_f32 v29, v148, v149
	global_store_dwordx4 v[156:157], v[26:29], off offset:256
	s_waitcnt vmcnt(14)
	s_nop 0
	v_lshlrev_b32_e32 v26, 16, v22
	v_and_b32_e32 v27, 0xffff0000, v22
	v_pk_fma_f32 v[26:27], v[144:145], v[198:199], v[26:27]
	s_nop 0
	v_cvt_pk_bf16_f32 v22, v26, v27
	v_lshlrev_b32_e32 v26, 16, v23
	v_and_b32_e32 v27, 0xffff0000, v23
	v_pk_fma_f32 v[26:27], v[146:147], v[196:197], v[26:27]
	s_nop 0
	v_cvt_pk_bf16_f32 v23, v26, v27
	v_lshlrev_b32_e32 v26, 16, v24
	v_and_b32_e32 v27, 0xffff0000, v24
	v_pk_fma_f32 v[26:27], v[140:141], v[192:193], v[26:27]
	s_nop 0
	v_cvt_pk_bf16_f32 v24, v26, v27
	v_lshlrev_b32_e32 v26, 16, v25
	v_and_b32_e32 v27, 0xffff0000, v25
	v_pk_fma_f32 v[26:27], v[142:143], v[174:175], v[26:27]
	s_nop 0
	v_cvt_pk_bf16_f32 v25, v26, v27
	v_lshl_add_u64 v[26:27], s[80:81], 0, v[210:211]
	v_lshl_add_u64 v[26:27], v[26:27], 0, v[200:201]
	global_store_dwordx4 v[26:27], v[22:25], off
	s_waitcnt vmcnt(14)
	s_nop 0
	v_lshlrev_b32_e32 v22, 16, v18
	v_and_b32_e32 v23, 0xffff0000, v18
	v_pk_fma_f32 v[22:23], v[136:137], v[194:195], v[22:23]
	s_nop 0
	v_cvt_pk_bf16_f32 v18, v22, v23
	v_lshlrev_b32_e32 v22, 16, v19
	v_and_b32_e32 v23, 0xffff0000, v19
	v_pk_fma_f32 v[22:23], v[138:139], v[190:191], v[22:23]
	s_nop 0
	v_cvt_pk_bf16_f32 v19, v22, v23
	v_lshlrev_b32_e32 v22, 16, v20
	v_and_b32_e32 v23, 0xffff0000, v20
	v_pk_fma_f32 v[22:23], v[128:129], v[32:33], v[22:23]
	s_nop 0
	v_cvt_pk_bf16_f32 v20, v22, v23
	v_lshlrev_b32_e32 v22, 16, v21
	v_and_b32_e32 v23, 0xffff0000, v21
	v_pk_fma_f32 v[22:23], v[130:131], v[30:31], v[22:23]
	s_nop 0
	v_cvt_pk_bf16_f32 v21, v22, v23
	global_store_dwordx4 v[26:27], v[18:21], off offset:256
	s_waitcnt vmcnt(14)
	s_nop 0
	v_lshlrev_b32_e32 v18, 16, v14
	v_and_b32_e32 v19, 0xffff0000, v14
	v_pk_fma_f32 v[18:19], v[132:133], v[198:199], v[18:19]
	s_nop 0
	v_cvt_pk_bf16_f32 v14, v18, v19
	v_lshlrev_b32_e32 v18, 16, v15
	v_and_b32_e32 v19, 0xffff0000, v15
	v_pk_fma_f32 v[18:19], v[134:135], v[196:197], v[18:19]
	s_nop 0
	v_cvt_pk_bf16_f32 v15, v18, v19
	v_lshlrev_b32_e32 v18, 16, v16
	v_and_b32_e32 v19, 0xffff0000, v16
	v_pk_fma_f32 v[18:19], v[124:125], v[192:193], v[18:19]
	s_nop 0
	v_cvt_pk_bf16_f32 v16, v18, v19
	v_lshlrev_b32_e32 v18, 16, v17
	v_and_b32_e32 v19, 0xffff0000, v17
	v_pk_fma_f32 v[18:19], v[126:127], v[174:175], v[18:19]
	s_nop 0
	v_cvt_pk_bf16_f32 v17, v18, v19
	v_lshl_add_u64 v[18:19], s[80:81], 0, v[208:209]
	v_lshl_add_u64 v[18:19], v[18:19], 0, v[200:201]
	global_store_dwordx4 v[18:19], v[14:17], off
	s_waitcnt vmcnt(14)
	s_nop 0
	v_lshlrev_b32_e32 v14, 16, v10
	v_and_b32_e32 v15, 0xffff0000, v10
	v_pk_fma_f32 v[14:15], v[120:121], v[194:195], v[14:15]
	s_nop 0
	v_cvt_pk_bf16_f32 v10, v14, v15
	v_lshlrev_b32_e32 v14, 16, v11
	v_and_b32_e32 v15, 0xffff0000, v11
	v_pk_fma_f32 v[14:15], v[122:123], v[190:191], v[14:15]
	s_nop 0
	v_cvt_pk_bf16_f32 v11, v14, v15
	v_lshlrev_b32_e32 v14, 16, v12
	v_and_b32_e32 v15, 0xffff0000, v12
	v_pk_fma_f32 v[14:15], v[112:113], v[32:33], v[14:15]
	s_nop 0
	v_cvt_pk_bf16_f32 v12, v14, v15
	v_lshlrev_b32_e32 v14, 16, v13
	v_and_b32_e32 v15, 0xffff0000, v13
	v_pk_fma_f32 v[14:15], v[114:115], v[30:31], v[14:15]
	s_nop 0
	v_cvt_pk_bf16_f32 v13, v14, v15
	global_store_dwordx4 v[18:19], v[10:13], off offset:256
	s_waitcnt vmcnt(14)
	s_nop 0
	v_lshlrev_b32_e32 v10, 16, v6
	v_and_b32_e32 v11, 0xffff0000, v6
	v_pk_fma_f32 v[10:11], v[116:117], v[198:199], v[10:11]
	s_nop 0
	v_cvt_pk_bf16_f32 v6, v10, v11
	v_lshlrev_b32_e32 v10, 16, v7
	v_and_b32_e32 v11, 0xffff0000, v7
	v_pk_fma_f32 v[10:11], v[118:119], v[196:197], v[10:11]
	s_nop 0
	v_cvt_pk_bf16_f32 v7, v10, v11
	v_lshlrev_b32_e32 v10, 16, v8
	v_and_b32_e32 v11, 0xffff0000, v8
	v_pk_fma_f32 v[10:11], v[108:109], v[192:193], v[10:11]
	s_nop 0
	v_cvt_pk_bf16_f32 v8, v10, v11
	v_lshlrev_b32_e32 v10, 16, v9
	v_and_b32_e32 v11, 0xffff0000, v9
	v_pk_fma_f32 v[10:11], v[110:111], v[174:175], v[10:11]
	s_nop 0
	v_cvt_pk_bf16_f32 v9, v10, v11
	v_lshl_add_u64 v[10:11], s[80:81], 0, v[206:207]
	v_lshl_add_u64 v[10:11], v[10:11], 0, v[200:201]
	global_store_dwordx4 v[10:11], v[6:9], off
	s_waitcnt vmcnt(14)
	s_nop 0
	v_lshlrev_b32_e32 v6, 16, v2
	v_and_b32_e32 v7, 0xffff0000, v2
	v_pk_fma_f32 v[6:7], v[104:105], v[194:195], v[6:7]
	v_lshl_add_u64 v[104:105], v[204:205], 0, s[22:23]
	v_cvt_pk_bf16_f32 v2, v6, v7
	v_lshlrev_b32_e32 v6, 16, v3
	v_and_b32_e32 v7, 0xffff0000, v3
	v_pk_fma_f32 v[6:7], v[106:107], v[190:191], v[6:7]
	s_mov_b64 s[22:23], 0x48000
	v_cvt_pk_bf16_f32 v3, v6, v7
	v_lshlrev_b32_e32 v6, 16, v4
	v_and_b32_e32 v7, 0xffff0000, v4
	v_pk_fma_f32 v[6:7], v[100:101], v[32:33], v[6:7]
	v_lshl_add_u64 v[106:107], v[204:205], 0, s[22:23]
	v_cvt_pk_bf16_f32 v4, v6, v7
	v_lshlrev_b32_e32 v6, 16, v5
	v_and_b32_e32 v7, 0xffff0000, v5
	v_pk_fma_f32 v[6:7], v[102:103], v[30:31], v[6:7]
	s_mov_b64 s[22:23], 0x50000
	v_cvt_pk_bf16_f32 v5, v6, v7
	global_store_dwordx4 v[10:11], v[2:5], off offset:256
	v_lshl_add_u64 v[108:109], v[204:205], 0, s[22:23]
	s_mov_b64 s[22:23], 0x58000
	v_lshl_add_u64 v[2:3], v[202:203], 0, v[104:105]
	s_waitcnt vmcnt(8)
	v_mov_b64_e32 v[6:7], v[212:213]
	v_mov_b64_e32 v[8:9], v[214:215]
	v_mov_b64_e32 v[10:11], v[216:217]
	v_mov_b64_e32 v[12:13], v[218:219]
	v_lshl_add_u64 v[2:3], v[202:203], 0, v[106:107]
	v_mov_b64_e32 v[14:15], v[224:225]
	v_mov_b64_e32 v[16:17], v[226:227]
	v_mov_b64_e32 v[18:19], v[228:229]
	v_mov_b64_e32 v[20:21], v[230:231]
	v_lshl_add_u64 v[2:3], v[202:203], 0, v[108:109]
	v_mov_b64_e32 v[22:23], v[232:233]
	v_mov_b64_e32 v[24:25], v[234:235]
	v_mov_b64_e32 v[26:27], v[236:237]
	v_mov_b64_e32 v[28:29], v[238:239]
	v_lshl_add_u64 v[110:111], v[204:205], 0, s[22:23]
	v_lshl_add_u64 v[2:3], v[202:203], 0, v[110:111]
	v_mov_b64_e32 v[100:101], v[240:241]
	v_mov_b64_e32 v[102:103], v[242:243]
	s_nop 0
	global_load_dwordx4 v[2:5], v[2:3], off offset:256
	s_mov_b64 s[22:23], -1
	s_waitcnt vmcnt(7)
	v_lshlrev_b32_e32 v112, 16, v6
	v_and_b32_e32 v113, 0xffff0000, v6
	v_pk_fma_f32 v[96:97], v[96:97], v[198:199], v[112:113]
	s_nop 0
	v_cvt_pk_bf16_f32 v6, v96, v97
	v_lshlrev_b32_e32 v96, 16, v7
	v_and_b32_e32 v97, 0xffff0000, v7
	v_pk_fma_f32 v[96:97], v[98:99], v[196:197], v[96:97]
	s_nop 0
	v_cvt_pk_bf16_f32 v7, v96, v97
	v_lshlrev_b32_e32 v96, 16, v8
	v_and_b32_e32 v97, 0xffff0000, v8
	v_pk_fma_f32 v[92:93], v[92:93], v[192:193], v[96:97]
	s_nop 0
	v_cvt_pk_bf16_f32 v8, v92, v93
	v_lshlrev_b32_e32 v92, 16, v9
	v_and_b32_e32 v93, 0xffff0000, v9
	v_pk_fma_f32 v[92:93], v[94:95], v[174:175], v[92:93]
	s_nop 0
	v_cvt_pk_bf16_f32 v9, v92, v93
	v_lshl_add_u64 v[92:93], s[80:81], 0, v[104:105]
	v_lshl_add_u64 v[92:93], v[92:93], 0, v[200:201]
	global_store_dwordx4 v[92:93], v[6:9], off
	s_waitcnt vmcnt(7)
	s_nop 0
	v_lshlrev_b32_e32 v6, 16, v10
	v_and_b32_e32 v7, 0xffff0000, v10
	v_lshlrev_b32_e32 v8, 16, v11
	v_and_b32_e32 v9, 0xffff0000, v11
	v_pk_fma_f32 v[6:7], v[88:89], v[194:195], v[6:7]
	v_pk_fma_f32 v[8:9], v[90:91], v[190:191], v[8:9]
	v_cvt_pk_bf16_f32 v6, v6, v7
	v_cvt_pk_bf16_f32 v7, v8, v9
	v_lshlrev_b32_e32 v8, 16, v12
	v_and_b32_e32 v9, 0xffff0000, v12
	v_lshlrev_b32_e32 v10, 16, v13
	v_and_b32_e32 v11, 0xffff0000, v13
	v_pk_fma_f32 v[8:9], v[80:81], v[32:33], v[8:9]
	v_pk_fma_f32 v[10:11], v[82:83], v[30:31], v[10:11]
	v_cvt_pk_bf16_f32 v8, v8, v9
	v_cvt_pk_bf16_f32 v9, v10, v11
	global_store_dwordx4 v[92:93], v[6:9], off offset:256
	s_waitcnt vmcnt(7)
	v_lshlrev_b32_e32 v10, 16, v17
	v_and_b32_e32 v11, 0xffff0000, v17
	v_lshlrev_b32_e32 v6, 16, v14
	v_and_b32_e32 v7, 0xffff0000, v14
	v_lshlrev_b32_e32 v8, 16, v15
	v_and_b32_e32 v9, 0xffff0000, v15
	v_pk_fma_f32 v[6:7], v[84:85], v[198:199], v[6:7]
	v_pk_fma_f32 v[8:9], v[86:87], v[196:197], v[8:9]
	v_cvt_pk_bf16_f32 v6, v6, v7
	v_cvt_pk_bf16_f32 v7, v8, v9
	v_lshlrev_b32_e32 v8, 16, v16
	v_and_b32_e32 v9, 0xffff0000, v16
	v_pk_fma_f32 v[8:9], v[76:77], v[192:193], v[8:9]
	v_pk_fma_f32 v[10:11], v[78:79], v[174:175], v[10:11]
	v_cvt_pk_bf16_f32 v8, v8, v9
	v_cvt_pk_bf16_f32 v9, v10, v11
	v_lshl_add_u64 v[10:11], s[80:81], 0, v[106:107]
	v_lshl_add_u64 v[10:11], v[10:11], 0, v[200:201]
	global_store_dwordx4 v[10:11], v[6:9], off
	s_waitcnt vmcnt(7)
	v_lshlrev_b32_e32 v12, 16, v21
	v_and_b32_e32 v13, 0xffff0000, v21
	v_lshlrev_b32_e32 v6, 16, v18
	v_and_b32_e32 v7, 0xffff0000, v18
	v_lshlrev_b32_e32 v8, 16, v19
	v_and_b32_e32 v9, 0xffff0000, v19
	v_pk_fma_f32 v[6:7], v[72:73], v[194:195], v[6:7]
	v_pk_fma_f32 v[8:9], v[74:75], v[190:191], v[8:9]
	v_cvt_pk_bf16_f32 v6, v6, v7
	v_cvt_pk_bf16_f32 v7, v8, v9
	v_lshlrev_b32_e32 v8, 16, v20
	v_and_b32_e32 v9, 0xffff0000, v20
	v_pk_fma_f32 v[8:9], v[64:65], v[32:33], v[8:9]
	v_pk_fma_f32 v[12:13], v[66:67], v[30:31], v[12:13]
	v_cvt_pk_bf16_f32 v8, v8, v9
	v_cvt_pk_bf16_f32 v9, v12, v13
	global_store_dwordx4 v[10:11], v[6:9], off offset:256
	s_waitcnt vmcnt(7)
	v_lshlrev_b32_e32 v10, 16, v25
	v_and_b32_e32 v11, 0xffff0000, v25
	v_lshlrev_b32_e32 v6, 16, v22
	v_and_b32_e32 v7, 0xffff0000, v22
	v_lshlrev_b32_e32 v8, 16, v23
	v_and_b32_e32 v9, 0xffff0000, v23
	v_pk_fma_f32 v[6:7], v[68:69], v[198:199], v[6:7]
	v_pk_fma_f32 v[8:9], v[70:71], v[196:197], v[8:9]
	v_cvt_pk_bf16_f32 v6, v6, v7
	v_cvt_pk_bf16_f32 v7, v8, v9
	v_lshlrev_b32_e32 v8, 16, v24
	v_and_b32_e32 v9, 0xffff0000, v24
	v_pk_fma_f32 v[8:9], v[60:61], v[192:193], v[8:9]
	v_pk_fma_f32 v[10:11], v[62:63], v[174:175], v[10:11]
	v_cvt_pk_bf16_f32 v8, v8, v9
	v_cvt_pk_bf16_f32 v9, v10, v11
	v_lshl_add_u64 v[10:11], s[80:81], 0, v[108:109]
	v_lshl_add_u64 v[10:11], v[10:11], 0, v[200:201]
	global_store_dwordx4 v[10:11], v[6:9], off
	s_waitcnt vmcnt(7)
	v_lshlrev_b32_e32 v12, 16, v29
	v_and_b32_e32 v13, 0xffff0000, v29
	v_lshlrev_b32_e32 v6, 16, v26
	v_and_b32_e32 v7, 0xffff0000, v26
	v_lshlrev_b32_e32 v8, 16, v27
	v_and_b32_e32 v9, 0xffff0000, v27
	v_pk_fma_f32 v[6:7], v[56:57], v[194:195], v[6:7]
	v_pk_fma_f32 v[8:9], v[58:59], v[190:191], v[8:9]
	v_cvt_pk_bf16_f32 v6, v6, v7
	v_cvt_pk_bf16_f32 v7, v8, v9
	v_lshlrev_b32_e32 v8, 16, v28
	v_and_b32_e32 v9, 0xffff0000, v28
	v_pk_fma_f32 v[8:9], v[48:49], v[32:33], v[8:9]
	v_pk_fma_f32 v[12:13], v[50:51], v[30:31], v[12:13]
	v_cvt_pk_bf16_f32 v8, v8, v9
	v_cvt_pk_bf16_f32 v9, v12, v13
	global_store_dwordx4 v[10:11], v[6:9], off offset:256
	s_waitcnt vmcnt(7)
	v_lshlrev_b32_e32 v10, 16, v103
	v_and_b32_e32 v11, 0xffff0000, v103
	v_lshlrev_b32_e32 v6, 16, v100
	v_and_b32_e32 v7, 0xffff0000, v100
	v_lshlrev_b32_e32 v8, 16, v101
	v_and_b32_e32 v9, 0xffff0000, v101
	v_pk_fma_f32 v[6:7], v[52:53], v[198:199], v[6:7]
	v_pk_fma_f32 v[8:9], v[54:55], v[196:197], v[8:9]
	v_cvt_pk_bf16_f32 v6, v6, v7
	v_cvt_pk_bf16_f32 v7, v8, v9
	v_lshlrev_b32_e32 v8, 16, v102
	v_and_b32_e32 v9, 0xffff0000, v102
	v_pk_fma_f32 v[8:9], v[44:45], v[192:193], v[8:9]
	v_pk_fma_f32 v[10:11], v[46:47], v[174:175], v[10:11]
	v_cvt_pk_bf16_f32 v8, v8, v9
	v_cvt_pk_bf16_f32 v9, v10, v11
	v_lshl_add_u64 v[10:11], s[80:81], 0, v[110:111]
	v_lshl_add_u64 v[10:11], v[10:11], 0, v[200:201]
	global_store_dwordx4 v[10:11], v[6:9], off
	s_waitcnt vmcnt(7)
	s_nop 0
	v_lshlrev_b32_e32 v6, 16, v2
	v_and_b32_e32 v7, 0xffff0000, v2
	v_pk_fma_f32 v[6:7], v[40:41], v[194:195], v[6:7]
	s_nop 0
	v_cvt_pk_bf16_f32 v2, v6, v7
	v_lshlrev_b32_e32 v6, 16, v3
	v_and_b32_e32 v7, 0xffff0000, v3
	v_pk_fma_f32 v[6:7], v[42:43], v[190:191], v[6:7]
	s_nop 0
	v_cvt_pk_bf16_f32 v3, v6, v7
	v_lshlrev_b32_e32 v6, 16, v4
	v_and_b32_e32 v7, 0xffff0000, v4
	v_pk_fma_f32 v[6:7], v[36:37], v[32:33], v[6:7]
	s_nop 0
	v_cvt_pk_bf16_f32 v4, v6, v7
	v_lshlrev_b32_e32 v6, 16, v5
	v_and_b32_e32 v7, 0xffff0000, v5
	v_pk_fma_f32 v[6:7], v[38:39], v[30:31], v[6:7]
	s_nop 0
	v_cvt_pk_bf16_f32 v5, v6, v7
	global_store_dwordx4 v[10:11], v[2:5], off offset:256
	s_cbranch_vccnz .LBB0_1152
	s_andn2_b64 vcc, exec, s[6:7]
	s_cbranch_vccnz .LBB0_1151
	s_barrier
	s_branch .LBB0_1151
